# baseline (speedup 1.0000x reference)
_Z5k_midPKfPKtPKiS4_PtS4_S4_S4_S4_PiS6_S6_S6_S4_S6_S6_:
	s_load_dwordx2 s[6:7], s[0:1], 0x10
	s_cmpk_gt_i32 s2, 0xfb
	s_mov_b64 s[4:5], -1
	s_cbranch_scc0 .LBB1_55
	s_cmpk_gt_u32 s2, 0x1bf
	s_cbranch_scc0 .LBB1_15
	v_cmp_gt_u32_e32 vcc, 16, v0
	s_and_saveexec_b64 s[4:5], vcc
	v_mov_b32_e32 v1, 0x24000
	v_lshl_or_b32 v1, v0, 2, v1
	v_mov_b32_e32 v2, 0
	ds_write_b32 v1, v2
	s_or_b64 exec, exec, s[4:5]
	s_load_dwordx2 s[8:9], s[0:1], 0x78
	s_load_dwordx2 s[10:11], s[0:1], 0x68
	s_movk_i32 s4, 0x240
	s_add_i32 s3, s2, 0xfffffe40
	v_cmp_gt_u32_e32 vcc, s4, v0
	s_waitcnt lgkmcnt(0)
	v_lshl_or_b32 v118, s3, 10, v0
	s_mov_b32 s20, 0x186a0
	v_cmp_gt_u32_e64 s[14:15], s20, v118
	s_and_saveexec_b64 s[16:17], s[14:15]
	v_lshlrev_b32_e32 v118, 2, v118
	global_load_dword v117, v118, s[10:11]
	s_mov_b64 exec, s[16:17]
	s_barrier
	s_and_saveexec_b64 s[12:13], vcc
	s_cbranch_execz .LBB1_10
	s_load_dwordx2 s[14:15], s[0:1], 0x70
	v_lshrrev_b32_e32 v6, 6, v0
	v_and_b32_e32 v7, 63, v0
	v_lshlrev_b32_e32 v1, 2, v6
	v_lshl_or_b32 v2, v7, 6, v1
	v_mov_b32_e32 v3, 0
	v_lshl_add_u64 v[4:5], s[6:7], 0, v[2:3]
	s_mov_b64 s[16:17], 0
	s_mov_b64 s[18:19], 0x1000
	v_mov_b32_e32 v2, v3
	v_mov_b32_e32 v8, v7

.LBB1_10:
	s_or_b64 exec, exec, s[12:13]
	v_lshl_or_b32 v2, s3, 10, v0
	s_mov_b32 s3, 0x186a0
	v_cmp_gt_u32_e32 vcc, s3, v2
	s_waitcnt lgkmcnt(0)
	v_mov_b64_e32 v[4:5], 0
	v_mov_b32_e32 v1, -1
	s_and_saveexec_b64 s[4:5], vcc
	s_cbranch_execz .LBB1_12
	v_mov_b32_e32 v3, 0
	s_mov_b32 s3, 0x38e38e39
	v_mov_b32_e32 v3, 1
	s_waitcnt vmcnt(0)
	v_mov_b32_e32 v1, v117
	v_mul_hi_i32 v4, v1, s3
	v_lshrrev_b32_e32 v5, 31, v4
	v_ashrrev_i32_e32 v4, 1, v4
	v_add_u32_e32 v4, v4, v5
	v_lshl_add_u32 v4, v4, 3, v4
	v_sub_u32_e32 v1, v1, v4
	v_add_u32_e32 v4, 9, v1
	v_cmp_gt_i32_e32 vcc, 0, v1
	s_nop 1
	v_cndmask_b32_e32 v1, v1, v4, vcc
	v_mov_b32_e32 v4, 0x24000
	v_lshl_add_u32 v4, v1, 2, v4
	ds_add_rtn_u32 v4, v4, v3
	s_waitcnt lgkmcnt(0)
	v_ashrrev_i32_e32 v5, 31, v4
